# GU tail units moved behind the GU/DN grid barrier (tail WGs re-enter GU, signal counter; DN remapped)
# speedup vs baseline: 1.0122x; 1.0122x over previous
; #define LAS __attribute__((address_space(3)))
; __device__ __forceinline__ int opaque_tid() { int t = threadIdx.x; asm volatile("" : "+v"(t)); return t; }
;     __device__ __forceinline__ bool next(int i, Unit& u) const {
;         const long L = (long)i * G + c; if (L >= nwg) return false;
;         int wgid = (int)L; { const int q = nwg / NXCD, r = nwg % NXCD, xcd = wgid % NXCD, off = wgid / NXCD; wgid = (xcd < r ? xcd * (q + 1) : r * (q + 1) + (xcd - r) * q) + off; }
;         const int nig = WGM * nN, gid = wgid / nig, fm = gid * WGM, gsz = (nM - fm) < WGM ? (nM - fm) : WGM;
;         u.pm = fm + ((wgid % nig) % gsz); u.pn = (wgid % nig) / gsz; u.e = 0; u.rows = 256;
;         u.a = A + (size_t)u.pm * tstepA; u.b = Bt + (size_t)u.pn * tstep; return true;
; __device__ __forceinline__ void pj_mfma(const Args& a, LAS unsigned char* lds, int layer) {
;     pg8::DenseOrder So; So.init(a.ws + WS_ACT, a.ws + WS_WIN + (size_t)layer * 3328 * D * 2, NTOK, 3328, D, gridDim.x, blockIdx.x);
;     LAS float* gl = (LAS float*)(lds + SEG_OFF + 256);
;     { const int t_ = opaque_tid(); if (t_ < 256) { const int w = t_ >> 6, i = t_ & 63; const float* gp_ = w == 0 ? a.in[I_QGF] : w == 1 ? a.in[I_KGF] : w == 2 ? a.in[I_QGD] : a.in[I_KGD]; gl[t_] = gp_[layer * 64 + i]; } }
;     __syncthreads();
;     EpiProj E{(bf16_t*)(a.ws + WS_PROJ), gl};
;     pg8::gemm_phase<EpiProj, pg8::DenseOrder>(lds, D, So, E);
;     if ((int)blockIdx.x >= (int)gridDim.x - 32) cumsum_unit(a, lds, blockIdx.x - (gridDim.x - 32));
;     if (layer + 1 < NL) { __syncthreads(); constexpr int I_SPLIT = 10240;
;         const int half = gridDim.x / 2; const bool upper = (int)blockIdx.x >= half;
;         p0_prep(a, lds, layer + 1, upper ? half : 0, upper ? (int)gridDim.x - half : half, upper ? 0 : I_SPLIT, upper ? I_SPLIT : (1 << 30)); }
.LBB0_101:
	s_or_b64 exec, exec, s[0:1]
	s_mov_b32 vcc_lo, 0
	s_nop 1
	v_writelane_b32 v254, vcc_lo, 62
	s_nop 1
	s_waitcnt lgkmcnt(0)
	s_barrier
	s_load_dwordx2 s[92:93], s[54:55], 0xa0
	s_load_dwordx16 s[12:27], s[54:55], 0x20
	s_load_dwordx4 s[0:3], s[54:55], 0x90
	s_movk_i32 s5, 0xd1
	s_mov_b32 s67, 0
	s_waitcnt vmcnt(0)
	v_mbcnt_lo_u32_b32 v1, -1, 0
	v_mbcnt_hi_u32_b32 v199, -1, v1
	s_waitcnt lgkmcnt(0)
	v_writelane_b32 v252, s0, 8
	v_and_b32_e32 v240, 64, v199
	s_mul_hi_u32 s85, s77, 0x600
	v_writelane_b32 v252, s1, 9
	v_writelane_b32 v252, s2, 10
	v_writelane_b32 v252, s3, 11
	s_add_u32 s0, s92, 0x100000
	s_addc_u32 s1, s93, 0
	v_writelane_b32 v252, s0, 12
	s_add_u32 s96, s92, 0xbc00000
	s_addc_u32 s97, s93, 0
	v_writelane_b32 v252, s1, 13
	s_lshl_b32 s0, s61, 3
	s_add_u32 s10, s92, 0x180000
	s_addc_u32 s11, s93, 0
	s_add_u32 s80, s92, 0x7c00000
	s_addc_u32 s81, s93, 0
	v_writelane_b32 v252, s0, 14
	s_add_u32 s0, s92, 0xfc00000
	s_addc_u32 s1, s93, 0
	s_add_u32 s50, s92, 0x18c00000
	s_addc_u32 s51, s93, 0
	s_add_u32 s2, s92, 0xa00000
	s_addc_u32 s3, s93, 0
	v_writelane_b32 v252, s2, 15
	s_cmpk_lt_i32 s61, 0x680
	s_mul_i32 s84, s77, 0x600
	v_writelane_b32 v252, s3, 16
	s_cselect_b64 s[2:3], -1, 0
	v_writelane_b32 v252, s2, 17
	v_mov_b32_e32 v35, 0
	v_add_u32_e32 v241, 64, v240
	v_writelane_b32 v252, s3, 18
	s_ashr_i32 s2, s61, 31
	v_writelane_b32 v252, s2, 19
	s_lshr_b32 s2, s2, 29
	s_add_i32 s3, s61, s2
	s_ashr_i32 s2, s3, 3
	s_and_b32 s3, s3, -8
	s_sub_i32 s3, s61, s3
	s_lshl_b32 s4, s3, 6
	s_cmp_lt_i32 s3, 0
	s_cselect_b32 s5, s5, 0xd0
	s_mul_i32 s5, s5, s3
	s_mulk_i32 s3, 0x41
	s_cselect_b32 s3, s3, s4
	s_add_i32 s5, s5, s2
	s_mul_hi_i32 s4, s5, 0x4ec4ec4f
	s_lshr_b32 s6, s4, 31
	s_ashr_i32 s4, s4, 5
	s_add_i32 s4, s4, s6
	s_mul_i32 s6, s4, 0x68
	s_sub_i32 s5, s5, s6
	s_lshl_b32 s7, s4, 3
	s_bfe_i32 s4, s5, 0x80000
	s_bfe_u32 s4, s4, 0x3000c
	s_add_i32 s6, s5, s4
	s_bfe_i32 s4, s6, 0x80000
	s_and_b32 s6, s6, 0xf8
	s_sub_i32 s5, s5, s6
	s_sext_i32_i16 s8, s4
	s_sext_i32_i8 s5, s5
	s_add_i32 s28, s7, s5
	s_ashr_i32 s5, s8, 3
	v_writelane_b32 v252, s5, 20
	s_mov_b32 s6, s28
	s_ashr_i32 s29, s28, 31
	v_writelane_b32 v252, s6, 21
	s_lshr_b32 s4, s8, 3
	v_xor_b32_e32 v236, 16, v199
	v_writelane_b32 v252, s7, 22
	s_lshl_b64 s[6:7], s[28:29], 19
	s_add_u32 s6, s80, s6
	s_addc_u32 s7, s81, s7
	v_writelane_b32 v252, s6, 23
	s_bfe_i64 s[4:5], s[4:5], 0x100000
	s_lshl_b64 s[4:5], s[4:5], 19
	v_writelane_b32 v252, s7, 24
	v_writelane_b32 v252, s4, 25
	v_xor_b32_e32 v237, 32, v199
	v_mov_b32_e32 v238, 1
	v_writelane_b32 v252, s5, 26
	s_ashr_i32 s4, s77, 31
	v_writelane_b32 v252, s4, 27
	s_sub_i32 s4, s77, 32
	s_cmp_ge_i32 s61, s4
	s_cselect_b64 s[6:7], -1, 0
	v_writelane_b32 v252, s6, 28
	s_sub_i32 s4, s61, s4
	s_and_b32 s5, s4, 3
	v_writelane_b32 v252, s7, 29
	s_ashr_i32 s6, s4, 2
	s_ashr_i32 s7, s6, 31
	s_lshl_b32 s5, s5, 2
	s_add_u32 s5, s10, s5
	v_writelane_b32 v252, s10, 30
	s_addc_u32 s8, s11, 0
	s_lshl_b64 s[6:7], s[6:7], 16
	s_add_u32 s6, s5, s6
	s_addc_u32 s7, s8, s7
	s_add_u32 s28, s92, 0x200000
	s_addc_u32 s29, s93, 0
	s_ashr_i32 s5, s4, 31
	s_lshl_b64 s[4:5], s[4:5], 14
	v_writelane_b32 v252, s11, 31
	s_add_u32 s4, s28, s4
	v_writelane_b32 v252, s6, 32
	s_addc_u32 s5, s29, s5
	s_lshr_b32 s8, s77, 1
	v_writelane_b32 v252, s7, 33
	s_sub_i32 s9, s77, s8
	v_writelane_b32 v252, s4, 34
	s_cmp_lt_i32 s61, s8
	v_mov_b32_e32 v198, 0x358637bd
	v_writelane_b32 v252, s5, 35
	s_cselect_b64 s[4:5], -1, 0
	s_and_b64 s[6:7], s[4:5], exec
	s_cselect_b32 s6, s8, s9
	s_movk_i32 s7, 0x3880
	s_cselect_b32 s10, 0, s8
	s_cselect_b32 s8, 0x2800, 0
	s_cselect_b32 s7, s7, 0x2800
	s_lshl_b32 s6, s6, 3
	v_writelane_b32 v252, s7, 36
	s_cmp_ge_i32 s61, s10
	v_writelane_b32 v252, s6, 37
	s_cselect_b64 s[6:7], -1, 0
	s_or_b64 s[4:5], s[36:37], s[4:5]
	s_load_dwordx8 s[36:43], s[54:55], 0x60
	s_and_b64 s[4:5], s[6:7], s[4:5]
	v_writelane_b32 v252, s4, 38
	v_mov_b32_e32 v201, 1.0
	v_mov_b32_e32 v239, 0x7f800000
	v_writelane_b32 v252, s5, 39
	s_sub_i32 s4, s61, s10
	s_lshl_b32 s4, s4, 3
	s_add_i32 s4, s4, s8
	s_waitcnt lgkmcnt(0)
	s_mov_b64 s[8:9], s[40:41]
	v_writelane_b32 v252, s4, 40
	s_add_u32 s6, s38, 0x400000
	s_mov_b64 s[10:11], s[42:43]
	s_mov_b64 s[4:5], s[36:37]
	v_writelane_b32 v252, s4, 41
	v_mov_b32_e32 v202, 0x3f317218
	v_mov_b32_e32 v242, 0xff800000
	v_writelane_b32 v252, s5, 42
	v_writelane_b32 v252, s6, 43
	v_writelane_b32 v252, s7, 44
	v_writelane_b32 v252, s8, 45
	v_writelane_b32 v252, s9, 46
	v_writelane_b32 v252, s10, 47
	v_writelane_b32 v252, s11, 48
	s_addc_u32 s7, s39, 0
	v_writelane_b32 v252, s6, 49
	s_add_u32 s4, s16, 0xd04000
	s_movk_i32 s74, 0x1ff
	v_writelane_b32 v252, s7, 50
	v_writelane_b32 v252, s12, 51
	s_addc_u32 s5, s17, 0
	s_mov_b32 s76, 0x800000
	v_writelane_b32 v255, s25, 0
	v_writelane_b32 v255, s26, 1
	v_writelane_b32 v255, s27, 2
	v_writelane_b32 v255, s4, 3
	v_writelane_b32 v252, s13, 52
	v_writelane_b32 v252, s14, 53
	v_writelane_b32 v255, s5, 4
	s_add_u32 s4, s92, 0x5b00000
	s_addc_u32 s5, s93, 0
	v_writelane_b32 v255, s4, 5
	v_writelane_b32 v252, s15, 54
	v_writelane_b32 v252, s16, 55
	v_writelane_b32 v255, s5, 6
	s_add_u32 s4, s92, 0x1b00000
	s_addc_u32 s5, s93, 0
	s_add_u32 s82, s92, 0x700000
	v_writelane_b32 v255, s4, 7
	s_addc_u32 s83, s93, 0
	v_writelane_b32 v252, s17, 56
	v_writelane_b32 v255, s5, 8
	s_add_u32 s4, s92, 0x14000
	v_writelane_b32 v255, s4, 9
	s_addc_u32 s4, s93, 0
	s_add_i32 s6, s61, 0x900
	s_cmpk_lt_i32 s61, 0x200
	v_writelane_b32 v255, s4, 10
	s_cselect_b64 s[4:5], -1, 0
	v_writelane_b32 v255, s4, 11
	v_writelane_b32 v252, s18, 57
	v_writelane_b32 v252, s19, 58
	v_writelane_b32 v255, s5, 12
;     ...
;     auto prologue = [&](int u) {
;         if (!UNIT_ON(u)) return;
;         int lane = tid & 63; asm volatile("" : "+v"(lane));
;         const int r32 = lane & 31, hi = lane >> 5;
;         if (u < AT_NFOX) {
;             const int qb = 15 - (u >> 5), bh = u & 31, b = bh >> 2, h = bh & 3, q0 = qb * 256;
;             const size_t rb = (size_t)b * S;
;             const bf16_t* Kb = proj + ((size_t)(4 + h) * NTOK + rb) * 64;
;             const bf16_t* Vb = proj + ((size_t)(8 + h) * NTOK + rb) * 64;
;             const float* cum = cumall + (size_t)bh * S;
;             const int jhi = 4 * qb + 3;
;             fox_cr = cum[q0]; fox_cv = cum[64 * (lane <= jhi ? lane : jhi) + 63]; fox_cq = cum[q0 + 32 * wid + r32];
;             if (!(dbg & 1)) { FOX_ISSUE(0); FOX_ISSUE(1); FOX_ISSUE(2); }
;             const bf16_t* Q = proj + ((size_t)(0 + h) * NTOK + rb + q0 + 32 * wid + r32) * 64;
; #pragma unroll
;             for (int d0 = 0; d0 < 4; ++d0) qr[d0] = *(const bf16x8*)(Q + d0 * 16 + hi * 8);
;         } else if (u < AT_NFOX + AT_NDIL) {
;             const int v2 = u - AT_NFOX, bh = v2 % 48, rest = v2 / 48, b = bh / 6, h = bh % 6, p = rest >> 4, x = rest & 15;
;             const int dil = p == 0 ? 1 : p == 1 ? 4 : 16, res = x % dil, nb2 = x / dil;
;             const size_t rb = (size_t)b * S;
;             const bf16_t* Kb = proj + ((size_t)(22 + h) * NTOK + rb) * 64;
;             const bf16_t* Vb = proj + ((size_t)(28 + h) * NTOK + rb) * 64;
;             const int mk_base = 256 * nb2 - 128, tt_lo = nb2 == 0 ? 2 : 0;
;             const size_t rs = (size_t)64 * dil;
; #pragma unroll
;     ...
;             if (tid < 256) { const int st = tid - 64; tab[tid] = (st >= 0 && st <= 128) ? relb[t5_bucket(st * dil) * 6 + h] : -INFINITY; }
;             const size_t trow = (size_t)(256 * nb2 + 32 * wid + r32) * dil + res;
;             const bf16_t* Q = proj + ((size_t)(16 + h) * NTOK + rb + trow) * 64;
; #pragma unroll
;             for (int d0 = 0; d0 < 4; ++d0) qr[d0] = *(const bf16x8*)(Q + d0 * 16 + hi * 8);
;         } else {
;             const int v2 = u - AT_NFOX - AT_NDIL, qb = 15 - v2 / 48, bh = v2 % 48, b = bh / 6, h = bh % 6, q0 = qb * 256;
;             const size_t rb = (size_t)b * S;
;             const bf16_t* Kb = proj + ((size_t)(40 + h) * NTOK + rb) * 64;
;             const bf16_t* Vb = proj + ((size_t)(46 + h) * NTOK + rb) * 64;
	s_and_b64 s[4:5], s[4:5], exec
	s_cselect_b32 s13, s61, s6
	s_cmpk_lt_i32 s13, 0xe00
	s_cselect_b64 s[4:5], -1, 0
	v_writelane_b32 v255, s4, 13
	s_cmpk_gt_i32 s13, 0x1ff
	s_mov_b32 s17, s67
	v_writelane_b32 v255, s5, 14
	s_cselect_b64 s[4:5], -1, 0
	v_writelane_b32 v255, s4, 15
	s_cmpk_gt_u32 s13, 0xaff
	v_writelane_b32 v252, s20, 59
	v_writelane_b32 v255, s5, 16
	s_cselect_b64 s[4:5], -1, 0
	v_writelane_b32 v255, s4, 17
	v_writelane_b32 v252, s21, 60
	s_mov_b32 s21, s67
	v_writelane_b32 v255, s5, 18
	s_add_i32 s4, s13, 0xf500
	s_and_b32 s5, s4, 0xffff
	s_mul_i32 s5, s5, 0xaaab
	s_lshr_b32 s5, s5, 21
	s_mul_i32 s6, s5, 48
	s_sub_i32 s4, s4, s6
	s_and_b32 s6, s4, 0xff
	s_mulk_i32 s6, 0xab
	s_bfe_u32 s6, s6, 0x6000a
	s_mul_i32 s7, s6, 6
	s_sub_i32 s4, s4, s7
	s_and_b32 s4, s4, 0xff
	s_lshl_b32 s6, s6, 12
	s_lshl_b32 s4, s4, 15
	s_add_i32 s7, s6, s4
	s_lshl_b32 s7, s7, 7
	s_add_i32 s8, s7, 0xb800000
	s_add_u32 s8, s96, s8
	s_addc_u32 s9, s97, 0
	s_add_i32 s7, s7, 0xa000000
	s_add_u32 s7, s96, s7
	s_addc_u32 s10, s97, 0
	s_lshl_b32 s11, s5, 14
	s_sub_i32 s12, 0x3f000, s11
	s_lshl_b32 s12, s12, 1
	s_add_u32 s14, s7, s12
	s_addc_u32 s15, s10, 0
	v_writelane_b32 v255, s14, 19
	v_writelane_b32 v252, s22, 61
	v_writelane_b32 v252, s23, 62
	v_writelane_b32 v255, s15, 20
	s_add_u32 s14, s8, s12
	s_addc_u32 s15, s9, 0
	s_sub_i32 s12, 0x3e000, s11
	v_writelane_b32 v255, s14, 21
	s_lshl_b32 s12, s12, 1
	v_writelane_b32 v252, s24, 63
	v_writelane_b32 v255, s15, 22
	s_add_u32 s14, s7, s12
	s_addc_u32 s15, s10, 0
	v_writelane_b32 v255, s14, 23
	s_movk_i32 s56, 0x7f
	s_mov_b32 s57, 0xff800000
	v_writelane_b32 v255, s15, 24
	s_add_u32 s14, s8, s12
	s_addc_u32 s15, s9, 0
	s_sub_i32 s11, 0x3d000, s11
	v_writelane_b32 v255, s14, 25
	s_lshl_b32 s11, s11, 1
	s_mov_b32 s65, 0xc2ce8ed0
	v_writelane_b32 v255, s15, 26
	s_add_u32 s14, s7, s11
	s_addc_u32 s15, s10, 0
	s_add_u32 s8, s8, s11
	s_addc_u32 s9, s9, 0
	s_lshl_b32 s5, s5, 8
	s_sub_i32 s4, s4, s5
	s_add_i32 s5, s13, 0xfe00
	s_add_i32 s4, s4, s6
	s_and_b32 s6, s5, 0xffff
	s_mul_i32 s6, s6, 0xaaab
	s_lshr_b32 s7, s6, 21
	s_mul_i32 s7, s7, 48
	s_sub_i32 s5, s5, s7
	v_writelane_b32 v255, s14, 27
	s_and_b32 s7, s5, 0xff
	s_mulk_i32 s7, 0xab
	v_writelane_b32 v255, s15, 28
	v_writelane_b32 v255, s8, 29
	s_bfe_u32 s7, s7, 0x6000a
	s_add_i32 s4, s4, 0x110f00
	v_writelane_b32 v255, s9, 30
	s_mul_i32 s8, s7, 6
	s_sub_i32 s5, s5, s8
	s_and_b32 s5, s5, 0xff
	s_lshl_b32 s7, s7, 12
	s_lshl_b32 s8, s5, 15
	s_add_i32 s7, s7, s8
	v_writelane_b32 v255, s4, 31
	s_bfe_u32 s4, s6, 0x40015
	s_lshl_b32 s6, s7, 7
	s_add_u32 s6, s96, s6
	s_addc_u32 s8, s97, 0
	s_add_u32 s9, s6, 0x5800000
	s_addc_u32 s10, s8, 0
	s_add_u32 s6, s6, 0x7000000
	s_addc_u32 s8, s8, 0
	s_lshl_b32 s11, s4, 7
	s_or_b32 s12, s11, 0x60000
	s_add_u32 s14, s9, s12
	s_addc_u32 s15, s10, 0
	v_writelane_b32 v255, s14, 32
	s_mov_b64 s[44:45], -1
	s_mov_b64 s[86:87], 0x800
	v_writelane_b32 v255, s15, 33
	s_add_u32 s14, s6, s12
	s_addc_u32 s15, s8, 0
	v_writelane_b32 v255, s14, 34
	s_or_b32 s12, s11, 0x40000
	s_mov_b32 s60, 0xbfb8aa3b
	v_writelane_b32 v255, s15, 35
	s_add_u32 s14, s9, s12
	s_addc_u32 s15, s10, 0
	v_writelane_b32 v255, s14, 36
	s_mov_b64 s[88:89], 0x80
	s_mov_b64 s[94:95], 0x100
	v_writelane_b32 v255, s15, 37
	s_add_u32 s14, s6, s12
	s_addc_u32 s15, s8, 0
	v_writelane_b32 v255, s14, 38
	s_or_b32 s12, s11, 0x20000
	s_mov_b32 s62, s67
	v_writelane_b32 v255, s15, 39
	s_add_u32 s14, s9, s12
	s_addc_u32 s15, s10, 0
	v_writelane_b32 v255, s14, 40
	s_nop 1
	v_writelane_b32 v255, s15, 41
	s_add_u32 s14, s6, s12
	s_addc_u32 s15, s8, 0
	v_writelane_b32 v255, s14, 42
	s_nop 1
	v_writelane_b32 v255, s15, 43
	s_add_u32 s14, s9, s11
	s_addc_u32 s15, s10, 0
	v_writelane_b32 v255, s14, 44
	s_add_u32 s10, s6, s11
	s_addc_u32 s11, s8, 0
	v_writelane_b32 v255, s15, 45
	s_lshl_b32 s5, s5, 2
	v_writelane_b32 v255, s10, 46
	s_add_i32 s5, s5, 0
	s_add_i32 s5, s5, 0x21f00
	v_writelane_b32 v255, s11, 47
	v_writelane_b32 v255, s5, 48
	s_ashr_i32 s5, s13, 5
	s_or_b32 s4, s7, s4
	s_sub_i32 s5, 15, s5
	s_lshl_b32 s6, s13, 10
	s_and_b32 s7, s13, 31
	s_and_b32 s6, s6, 0x7000
	s_lshl_b32 s7, s7, 14
	s_or_b32 s14, s4, 0x80000
	s_and_b32 s8, s13, 3
	s_lshl_b32 s16, s5, 8
	s_add_u32 s18, s28, s7
	s_addc_u32 s19, s29, 0
	s_lshl_b32 s7, s5, 2
	v_writelane_b32 v255, s13, 49
	s_or_b32 s20, s7, 3
	s_lshl_b64 s[4:5], s[16:17], 2
	v_writelane_b32 v255, s28, 50
	s_add_u32 s4, s18, s4
	v_writelane_b32 v255, s29, 51
	s_addc_u32 s5, s19, s5
	v_writelane_b32 v255, s4, 52
	s_mov_b32 s15, s67
	s_nop 0
	v_writelane_b32 v255, s5, 53
	s_lshl_b32 s4, s8, 22
	s_lshl_b32 s5, s6, 7
	s_or_b32 s4, s5, s4
	s_add_u32 s4, s96, s4
	s_addc_u32 s5, s97, 0
	s_add_u32 s9, s4, 0x2000000
	s_addc_u32 s10, s5, 0
	s_add_u32 s11, s4, 0x1000000
	s_addc_u32 s12, s5, 0
	s_lshl_b64 s[4:5], s[20:21], 13
	s_add_u32 s22, s11, s4
	s_addc_u32 s23, s12, s5
	v_writelane_b32 v255, s22, 54
	s_add_u32 s4, s9, s4
	s_addc_u32 s5, s10, s5
	v_writelane_b32 v255, s23, 55
	v_writelane_b32 v255, s4, 56
	s_lshl_b32 s66, s20, 6
	s_nop 0
	v_writelane_b32 v255, s5, 57
	s_mov_b32 s4, s20
	v_writelane_b32 v255, s4, 58
	s_nop 1
	v_writelane_b32 v255, s5, 59
	s_lshl_b64 s[4:5], s[66:67], 2
	s_add_u32 s4, s18, s4
	s_addc_u32 s5, s19, s5
	v_writelane_b32 v255, s4, 60
; #define FOX_ISSUE(i) do { const int j_ = jhi - (i), bf_ = (i) & 3; dma_kv(lds, bf_, Kb + (size_t)j_ * 4096, Vb + (size_t)j_ * 4096, 64, wid, lane); \
;         glds4(cum + j_ * 64 + lane, (unsigned)__builtin_amdgcn_readfirstlane(l0 + L_CK + bf_ * 256)); } while (0)
;     ...
;         if (u < AT_NFOX) {
;             const int qb = 15 - (u >> 5), bh = u & 31, b = bh >> 2, h = bh & 3, q0 = qb * 256;
;             const size_t rb = (size_t)b * S;
;             const bf16_t* Kb = proj + ((size_t)(4 + h) * NTOK + rb) * 64;
;             const bf16_t* Vb = proj + ((size_t)(8 + h) * NTOK + rb) * 64;
;             const float* cum = cumall + (size_t)bh * S;
;             const int jhi = 4 * qb + 3;
;             fox_cr = cum[q0]; fox_cv = cum[64 * (lane <= jhi ? lane : jhi) + 63]; fox_cq = cum[q0 + 32 * wid + r32];
;             if (!(dbg & 1)) { FOX_ISSUE(0); FOX_ISSUE(1); FOX_ISSUE(2); }
;             const bf16_t* Q = proj + ((size_t)(0 + h) * NTOK + rb + q0 + 32 * wid + r32) * 64;
; #pragma unroll
;             for (int d0 = 0; d0 < 4; ++d0) qr[d0] = *(const bf16x8*)(Q + d0 * 16 + hi * 8);
	s_or_b32 s66, s7, 2
	s_nop 0
	v_writelane_b32 v255, s5, 61
	s_lshl_b64 s[4:5], s[66:67], 13
	s_add_u32 s20, s11, s4
	s_addc_u32 s21, s12, s5
	s_add_u32 s4, s9, s4
	s_addc_u32 s5, s10, s5
	v_writelane_b32 v253, s4, 0
	s_lshl_b32 s66, s66, 6
	v_writelane_b32 v255, s20, 62
	v_writelane_b32 v253, s5, 1
	s_lshl_b64 s[4:5], s[66:67], 2
	s_add_u32 s4, s18, s4
	s_addc_u32 s5, s19, s5
	v_writelane_b32 v253, s4, 2
	s_or_b32 s66, s7, 1
	v_writelane_b32 v255, s21, 63
	v_writelane_b32 v253, s5, 3
	s_lshl_b64 s[4:5], s[66:67], 13
	s_add_u32 s20, s11, s4
	s_addc_u32 s21, s12, s5
	v_writelane_b32 v253, s20, 4
	s_add_u32 s4, s9, s4
	s_addc_u32 s5, s10, s5
	v_writelane_b32 v253, s21, 5
	v_writelane_b32 v253, s4, 6
	s_lshl_b32 s66, s66, 6
	s_mov_b32 s9, s67
	v_writelane_b32 v253, s5, 7
	s_lshl_b64 s[4:5], s[66:67], 2
	s_add_u32 s4, s18, s4
	v_writelane_b32 v253, s18, 8
	s_addc_u32 s5, s19, s5
	s_nop 0
	v_writelane_b32 v253, s19, 9
	v_writelane_b32 v253, s4, 10
	s_nop 1
	v_writelane_b32 v253, s5, 11
	s_lshl_b32 s4, s8, 15
	s_or_b32 s4, s6, s4
	s_mov_b32 s6, s16
	v_writelane_b32 v253, s6, 12
	s_add_i32 s4, s4, s16
	s_mov_b32 s8, s77
	v_writelane_b32 v253, s7, 13
	s_mov_b32 s6, s61
	s_mov_b32 s7, s67
	v_writelane_b32 v253, s4, 14
	s_lshl_b64 s[4:5], s[6:7], 9
	s_lshl_b64 s[70:71], s[8:9], 9
	v_writelane_b32 v253, s4, 15
	s_nop 1
	v_writelane_b32 v253, s5, 16
	s_add_u32 s4, s92, 0x8c00000
	s_addc_u32 s5, s93, 0
	v_writelane_b32 v253, s4, 17
	s_nop 1
	v_writelane_b32 v253, s5, 18
	s_add_u32 s4, s92, 0x1700000
	v_writelane_b32 v253, s4, 19
	s_addc_u32 s4, s93, 0
	v_writelane_b32 v253, s4, 20
	s_add_u32 s4, s92, 0x10000
	v_writelane_b32 v253, s4, 21
	s_addc_u32 s4, s93, 0
	v_writelane_b32 v253, s4, 22
	s_add_u32 s4, s92, 0x300000
	s_addc_u32 s5, s93, 0
	v_writelane_b32 v253, s4, 23
	s_nop 1
	v_writelane_b32 v253, s5, 24
	s_add_u32 s4, s92, 0x500000
	s_addc_u32 s5, s93, 0
	v_writelane_b32 v253, s4, 25
	s_cmpk_lt_i32 s61, 0x100
	s_nop 0
	v_writelane_b32 v253, s5, 26
	s_cselect_b64 s[4:5], -1, 0
	v_writelane_b32 v253, s4, 27
	s_nop 1
	v_writelane_b32 v253, s5, 28
	s_add_u32 s4, s92, 0x14400000
	s_addc_u32 s5, s93, 0
	v_writelane_b32 v253, s4, 29
	s_nop 1
	v_writelane_b32 v253, s5, 30
	s_add_i32 s4, s77, s61
	v_writelane_b32 v253, s4, 31
	s_add_u32 s4, s92, 0x7c00080
	s_addc_u32 s5, s93, 0
	s_add_i32 s2, s3, s2
	s_ashr_i32 s3, s2, 31
	s_lshr_b32 s3, s3, 27
	v_writelane_b32 v253, s4, 32
	s_add_i32 s3, s2, s3
	s_nop 0
	v_writelane_b32 v253, s5, 33
	s_and_b32 s4, s3, 0xffe0
	s_sub_i32 s2, s2, s4
	s_bfe_i32 s4, s2, 0x80000
	s_bfe_u32 s4, s4, 0x3000c
	s_add_i32 s4, s2, s4
	s_and_b32 s5, s4, 0xf8
	s_sub_i32 s2, s2, s5
	s_ashr_i32 s3, s3, 5
	s_bfe_i32 s4, s4, 0x80000
	s_lshl_b32 s3, s3, 3
	s_sext_i32_i16 s4, s4
	s_sext_i32_i8 s2, s2
	s_add_i32 s10, s3, s2
	s_ashr_i32 s2, s4, 3
	v_writelane_b32 v253, s2, 34
	s_lshr_b32 s2, s4, 3
	s_mov_b32 s4, s10
	s_ashr_i32 s11, s10, 31
	v_writelane_b32 v253, s4, 35
	s_nop 1
	v_writelane_b32 v253, s5, 36
	s_lshl_b64 s[4:5], s[10:11], 15
	s_add_u32 s4, s80, s4
	s_addc_u32 s5, s81, s5
	v_writelane_b32 v253, s14, 37
	s_bfe_i64 s[2:3], s[2:3], 0x100000
	s_lshl_b64 s[2:3], s[2:3], 19
	v_writelane_b32 v253, s15, 38
	v_writelane_b32 v253, s2, 39
	s_nop 1
	v_writelane_b32 v253, s3, 40
	s_add_u32 s2, s4, 0x4000
	s_addc_u32 s3, s5, 0
	v_writelane_b32 v253, s2, 41
	s_nop 1
	v_writelane_b32 v253, s3, 42
	s_add_u32 s2, s4, 0x400000
	v_writelane_b32 v253, s4, 43
	s_addc_u32 s3, s5, 0
	s_lshl_b64 s[52:53], s[8:9], 10
	v_writelane_b32 v253, s5, 44
	v_writelane_b32 v253, s2, 45
	s_add_i32 s64, 0, 0x13000
	s_nop 0
	v_writelane_b32 v253, s3, 46
	s_lshl_b32 s2, s61, 7
	v_writelane_b32 v253, s2, 47
	s_lshl_b32 s2, s77, 7
	v_writelane_b32 v253, s2, 48
	s_mul_i32 s2, s77, 0x3000
	v_writelane_b32 v253, s2, 49
	s_add_i32 s2, 0, 0x21c20
	v_writelane_b32 v253, s2, 50
	s_add_i32 s2, 0, 0x21c24
	v_writelane_b32 v253, s2, 51
	s_add_i32 s2, 0, 0x21000
	v_writelane_b32 v253, s2, 52
	s_add_i32 s2, 0, 0x21100
	v_writelane_b32 v253, s2, 53
	s_add_i32 s2, 0, 0x21200
	v_writelane_b32 v253, s2, 54
	s_add_i32 s2, 0, 0x21504
	v_writelane_b32 v253, s2, 55
	s_add_i32 s2, 0, 0x15040
	v_writelane_b32 v253, s2, 56
	s_add_i32 s2, 0, 0x15000
	v_writelane_b32 v253, s2, 57
	s_add_i32 s2, 0, 0x21e80
	v_writelane_b32 v253, s2, 58
	s_add_i32 s2, 0, 0x21e10
	v_writelane_b32 v253, s2, 59
	s_add_i32 s2, 0, 0x21e20
	v_writelane_b32 v253, s2, 60
	s_add_i32 s2, 0, 0x21e30
	v_writelane_b32 v253, s2, 61
	v_writelane_b32 v253, s54, 62
	s_load_dwordx2 s[4:5], s[54:55], 0x0
	s_mov_b32 s3, 0x42b17218
	v_writelane_b32 v253, s55, 63
	s_waitcnt lgkmcnt(0)
	v_writelane_b32 v254, s4, 0
	s_nop 1
	v_writelane_b32 v254, s5, 1
	s_lshl_b64 s[4:5], s[8:9], 13
	v_writelane_b32 v254, s4, 2
	s_nop 1
	v_writelane_b32 v254, s5, 3
	v_writelane_b32 v254, s6, 4
	s_lshl_b64 s[4:5], s[6:7], 12
	s_nop 0
	v_writelane_b32 v254, s7, 5
	v_writelane_b32 v254, s4, 6
	s_nop 1
	v_writelane_b32 v254, s5, 7
	s_lshl_b64 s[4:5], s[8:9], 14
	v_writelane_b32 v254, s4, 8
	s_nop 1
	v_writelane_b32 v254, s5, 9
	v_writelane_b32 v254, s8, 10
	s_lshl_b64 s[4:5], s[8:9], 12
	s_nop 0
	v_writelane_b32 v254, s9, 11
	v_writelane_b32 v254, s4, 12
	s_nop 1
	v_writelane_b32 v254, s5, 13
	v_writelane_b32 v254, s82, 14
	s_nop 1
	v_writelane_b32 v254, s83, 15
	s_branch .LBB0_104

; #define LAS __attribute__((address_space(3)))
; __device__ __forceinline__ int opaque_tid() { int t = threadIdx.x; asm volatile("" : "+v"(t)); return t; }
; __device__ __forceinline__ void seg_to_lds(const Args& a, LAS unsigned char* lds, int layer) {
;     LAS int* seg = (LAS int*)(lds + SEG_OFF);
;     const int t = opaque_tid();
;     if (t < 16) {
;         unsigned* cnt = (unsigned*)(a.ws + WS_CTL) + CW_CNT + layer * 16 * 64;
;         const int c = (int)__hip_atomic_load(cnt + t * 64, __ATOMIC_RELAXED, __HIP_MEMORY_SCOPE_AGENT);
;         const int pad = (c + 255) & ~255;
;         int incl = pad;
; #pragma unroll
;         for (int o2 = 1; o2 < 16; o2 <<= 1) { const int u2 = __shfl_up(incl, o2); if (t >= o2) incl += u2; }
;         seg[t] = c; seg[16 + t] = incl - pad;
;         if (t == 15) seg[32] = incl;
;     }
;     __syncthreads();
; }
.Lgu_restart:
	v_mov_b32_e32 v1, v0
	s_waitcnt lgkmcnt(0)
	s_barrier
	s_nop 0
	v_cmp_gt_i32_e32 vcc, 16, v1
	s_and_saveexec_b64 s[4:5], vcc
	s_cbranch_execz .LBB0_901
	v_lshlrev_b32_e32 v2, 6, v1
	v_readlane_b32 s6, v254, 22
	v_ashrrev_i32_e32 v3, 31, v2
	v_readlane_b32 s7, v254, 23
	v_cmp_lt_i32_e32 vcc, v235, v240
	s_nop 0
	v_lshl_add_u64 v[2:3], v[2:3], 2, s[6:7]
	global_load_dword v3, v[2:3], off sc1
	s_waitcnt vmcnt(0)
	v_add_u32_e32 v2, 0xff, v3
	v_and_b32_e32 v4, 0xffffff00, v2
	v_cndmask_b32_e32 v2, v235, v199, vcc
	v_lshlrev_b32_e32 v2, 2, v2
	ds_bpermute_b32 v2, v2, v4
	v_cmp_lt_i32_e32 vcc, 0, v1
	s_waitcnt lgkmcnt(0)
	s_nop 0
	v_cndmask_b32_e32 v2, 0, v2, vcc
	v_cmp_lt_i32_e32 vcc, v233, v240
	v_add_u32_e32 v2, v4, v2
	s_nop 0
	v_cndmask_b32_e32 v5, v233, v199, vcc
	v_lshlrev_b32_e32 v5, 2, v5
	ds_bpermute_b32 v5, v5, v2
	v_cmp_lt_i32_e32 vcc, 1, v1
	s_waitcnt lgkmcnt(0)
	s_nop 0
	v_cndmask_b32_e32 v5, 0, v5, vcc
	v_cmp_lt_i32_e32 vcc, v243, v240
	v_add_u32_e32 v2, v2, v5
	s_nop 0
	v_cndmask_b32_e32 v5, v243, v199, vcc
	v_lshlrev_b32_e32 v5, 2, v5
	ds_bpermute_b32 v5, v5, v2
	v_cmp_lt_i32_e32 vcc, 3, v1
	s_waitcnt lgkmcnt(0)
	s_nop 0
	v_cndmask_b32_e32 v5, 0, v5, vcc
	v_cmp_lt_i32_e32 vcc, v203, v240
	v_add_u32_e32 v2, v2, v5
	s_nop 0
	v_cndmask_b32_e32 v5, v203, v199, vcc
	v_lshlrev_b32_e32 v5, 2, v5
	ds_bpermute_b32 v5, v5, v2
	v_cmp_lt_i32_e32 vcc, 7, v1
	s_waitcnt lgkmcnt(0)
	s_nop 0
	v_cndmask_b32_e32 v5, 0, v5, vcc
	v_add_u32_e32 v2, v2, v5
	v_lshl_add_u32 v5, v1, 2, 0
	v_add_u32_e32 v5, 0x21e00, v5
	v_sub_u32_e32 v4, v2, v4
	v_cmp_eq_u32_e32 vcc, 15, v1
	ds_write2_b32 v5, v3, v4 offset1:16
	s_and_b64 exec, exec, vcc
	s_cbranch_execz .LBB0_901
	v_readlane_b32 s2, v253, 58
	s_nop 1
	v_mov_b32_e32 v1, s2
	ds_write_b32 v1, v2

; #define LAS __attribute__((address_space(3)))
;     __device__ __forceinline__ bool next(int i, Unit& u) const {
;         int U = i * G + c, e = 0, found = 0, rem = 0;
;         typedef int i32x4 __attribute__((ext_vector_type(4)));
;         const i32x4 c0 = *(const LAS i32x4*)(seg), c1 = *(const LAS i32x4*)(seg + 4), c2 = *(const LAS i32x4*)(seg + 8), c3 = *(const LAS i32x4*)(seg + 12);
; #pragma unroll
;         for (int k = 0; k < 16; ++k) { const int ck = k < 4 ? c0[k & 3] : k < 8 ? c1[k & 3] : k < 12 ? c2[k & 3] : c3[k & 3];
;             const int nu = ((ck + 255) >> 8) * nct; if (!found) { if (U < nu) { found = 1; e = k; rem = U; } else U -= nu; } }
;         if (!found) return false;
;         e = __builtin_amdgcn_readfirstlane(e); rem = __builtin_amdgcn_readfirstlane(rem);
;         const int rt = rem / nct, ct = rem % nct;
;         u.e = e; u.pm = rt; u.pn = ct; u.rows = seg[e] - rt * 256;
;         u.a = A + (size_t)(seg[16 + e] + rt * 256) * arow_bytes; u.b = Bt + (size_t)e * bexp_bytes + (size_t)ct * btile_bytes; return true;
; template <class Epi, class Sched>
; __device__ __forceinline__ void gemm_phase_gather(LAS unsigned char* lds, const int K, const Sched& S, const Epi& E, const char* Ag, const int* list, const LAS int* seg) {
;     ...
;         Unit nx2; const bool has_nx2 = has_next && S.next(ui + 2, nx2);
;         if (has_nx2) PG8_ROWS(nx2, ca0, ca1); else { ca0[0] = na0[0]; ca0[1] = na0[1]; ca1[0] = na1[0]; ca1[1] = na1[1]; }
.LBB0_1039:
	s_mov_b64 s[8:9], 0
	s_and_b64 vcc, exec, s[20:21]
	s_cbranch_vccz .LBB0_1101
	v_mov_b32_e32 v34, s42
	ds_read_b128 v[134:137], v34
	s_add_i32 s4, s49, 2
	s_mul_i32 s4, s4, s77
	s_add_i32 s5, s4, s61
	s_lshl_b32 s4, s77, 2
	s_cmp_lt_u32 s5, s4
	s_cselect_b32 s5, s5, 0x100000
	v_readlane_b32 s4, v253, 59
	s_mov_b64 s[56:57], s[84:85]
	s_waitcnt lgkmcnt(0)
	v_readfirstlane_b32 s85, v136
	v_mov_b32_e32 v34, s4
	v_readfirstlane_b32 s84, v137
	ds_read_b128 v[136:139], v34
	v_readlane_b32 s4, v253, 60
	v_readfirstlane_b32 s8, v135
	s_waitcnt lgkmcnt(0)
	v_readfirstlane_b32 s63, v136
	v_mov_b32_e32 v34, s4
	v_readfirstlane_b32 s62, v137
	v_readfirstlane_b32 s95, v138
	v_readfirstlane_b32 s94, v139
	ds_read_b128 v[136:139], v34
	v_readlane_b32 s4, v253, 61
	s_waitcnt lgkmcnt(0)
	v_readfirstlane_b32 s79, v136
	v_mov_b32_e32 v34, s4
	v_readfirstlane_b32 s4, v134
	s_addk_i32 s4, 0xff
	s_ashr_i32 s4, s4, 6
	v_readfirstlane_b32 s78, v137
	v_readfirstlane_b32 s75, v138
	v_readfirstlane_b32 s41, v139
	ds_read_b128 v[136:139], v34
	s_and_b32 s9, s4, -4
	s_cmp_lt_i32 s5, s9
	s_cselect_b64 s[6:7], -1, 0
	s_and_b64 vcc, s[6:7], exec
	s_cselect_b32 s6, 0, s9
	s_waitcnt lgkmcnt(0)
	v_readfirstlane_b32 s40, v136
	v_readfirstlane_b32 s39, v137
	v_readfirstlane_b32 s38, v138
	v_readfirstlane_b32 s36, v139
	s_mov_b32 s4, 0
	s_sub_i32 s37, s5, s6
	s_mov_b64 s[6:7], 0
	s_cbranch_vccnz .LBB0_1052
	s_addk_i32 s8, 0xff
	s_ashr_i32 s4, s8, 6
	s_and_b32 s4, s4, -4
	s_cmp_lt_i32 s37, s4
	s_cbranch_scc1 .LBB0_1053
	s_sub_i32 s37, s37, s4
	s_mov_b32 s4, 0
	s_mov_b32 s5, 0
	s_branch .LBB0_1054

; __global__ void __launch_bounds__(NTHR, 2) mega_fwd(Args a) {
;     ...
;         gu_mfma(a, lds, layer);
;         xcd_barrier(bar);
;         dn_mfma(a, lds, layer);
;         xcd_barrier(bar);
.Ltail_signal:
	s_waitcnt vmcnt(0) lgkmcnt(0)
	s_barrier
	s_lshl_b32 vcc_hi, s77, 2
	s_sub_u32 s61, s61, vcc_hi
	v_readlane_b32 vcc_lo, v253, 31
	s_nop 1
	s_sub_u32 vcc_lo, vcc_lo, vcc_hi
	s_nop 1
	v_writelane_b32 v253, vcc_lo, 31
	s_nop 1
	s_mov_b32 vcc_lo, 0
	s_nop 1
	v_writelane_b32 v254, vcc_lo, 62
	s_nop 1
	v_cmp_eq_u32_e32 vcc, 0, v0
	s_and_saveexec_b64 s[4:5], vcc
	s_cbranch_execz .Ltail_sig_done
	buffer_wbl2 sc1
	s_waitcnt vmcnt(0)
	v_readlane_b32 s6, v254, 20
	s_nop 1
	s_lshl_b32 s6, s6, 2
	s_add_u32 s6, s6, 0x18000
	s_add_u32 s8, s92, s6
	s_addc_u32 s9, s93, 0
	v_mov_b32_e32 v1, 0
	v_mov_b32_e32 v2, 1
	global_atomic_add v1, v2, s[8:9]
	s_waitcnt vmcnt(0)
.Ltail_sig_done:
	s_or_b64 exec, exec, s[4:5]
	s_branch .Ldn_entry

; __device__ __forceinline__ void xcd_barrier(const XcdBarrier& b) {
;     asm volatile("s_waitcnt vmcnt(0)" ::: "memory");
;     __syncthreads();
;     if (threadIdx.x == 0) {
;         unsigned* bar = b.bar; unsigned bx = b.x;
;         asm volatile("" : "+s"(bar), "+s"(bx));
;         __builtin_amdgcn_s_waitcnt(0);
;         unsigned nloc = b.st[0], nx = b.st[1];
;         if (nloc == 0u) { xcd_barrier_complete(bar, bx, nloc, nx); b.st[0] = nloc; b.st[1] = nx; }
.LBB0_1112:
	v_readlane_b32 vcc_lo, v254, 62
	s_nop 1
	s_cmp_eq_u32 vcc_lo, 1
	s_cbranch_scc1 .Ltail_signal
	s_waitcnt vmcnt(0)
	s_waitcnt vmcnt(0)
	s_barrier
	s_mov_b64 s[36:37], exec
	v_readlane_b32 s4, v252, 3
	v_readlane_b32 s5, v252, 4
	s_and_b64 s[4:5], s[36:37], s[4:5]
	s_mov_b64 exec, s[4:5]
	s_cbranch_execz .LBB0_1156
	v_readlane_b32 s38, v252, 0
	v_readlane_b32 s4, v253, 50
	v_readlane_b32 s39, v252, 1
	v_readlane_b32 s2, v252, 2
	v_mov_b32_e32 v1, s4
	s_waitcnt vmcnt(0) expcnt(0) lgkmcnt(0)
	ds_read_b32 v4, v1
	v_readlane_b32 s4, v253, 51
	s_waitcnt lgkmcnt(0)
	v_cmp_ne_u32_e32 vcc, 0, v4
	v_mov_b32_e32 v1, s4
	ds_read_b32 v2, v1
	s_cbranch_vccnz .LBB0_1127
	v_readlane_b32 s4, v252, 5
	v_readlane_b32 s5, v252, 6
	s_load_dwordx2 s[8:9], s[4:5], 0x4
	s_add_u32 s4, s38, 0x1000
	s_addc_u32 s5, s39, 0
	s_add_u32 s6, s38, 0x1100
	s_addc_u32 s7, s39, 0
	s_waitcnt lgkmcnt(0)
	s_mul_i32 s30, s8, s77
	s_add_u32 s8, s38, 0x1200
	s_mul_i32 s30, s30, s9
	s_addc_u32 s9, s39, 0
	s_add_u32 s10, s38, 0x1300
	s_addc_u32 s11, s39, 0
	s_mov_b32 s31, 1
	s_mov_b64 s[12:13], 0
	s_branch .LBB0_1117

; #define LAS __attribute__((address_space(3)))
; __device__ __forceinline__ int opaque_tid() { int t = threadIdx.x; asm volatile("" : "+v"(t)); return t; }
; __device__ __forceinline__ void seg_to_lds(const Args& a, LAS unsigned char* lds, int layer) {
;     LAS int* seg = (LAS int*)(lds + SEG_OFF);
;     const int t = opaque_tid();
;     if (t < 16) {
;         unsigned* cnt = (unsigned*)(a.ws + WS_CTL) + CW_CNT + layer * 16 * 64;
;         const int c = (int)__hip_atomic_load(cnt + t * 64, __ATOMIC_RELAXED, __HIP_MEMORY_SCOPE_AGENT);
;         const int pad = (c + 255) & ~255;
;         int incl = pad;
; #pragma unroll
;         for (int o2 = 1; o2 < 16; o2 <<= 1) { const int u2 = __shfl_up(incl, o2); if (t >= o2) incl += u2; }
;         seg[t] = c; seg[16 + t] = incl - pad;
;         if (t == 15) seg[32] = incl;
;     }
;     __syncthreads();
; }
; __global__ void __launch_bounds__(NTHR, 2) mega_fwd(Args a) {
;     ...
;         gu_mfma(a, lds, layer);
;         xcd_barrier(bar);
;         dn_mfma(a, lds, layer);
.LBB0_1156:
	s_or_b64 exec, exec, s[36:37]
	v_mov_b32_e32 v1, 0x21e80
	ds_read_b32 v2, v1
	s_waitcnt lgkmcnt(0)
	v_readfirstlane_b32 vcc_lo, v2
	s_lshr_b32 vcc_lo, vcc_lo, 6
	s_lshl_b32 vcc_hi, s77, 2
	s_sub_i32 vcc_lo, vcc_lo, vcc_hi
	s_max_i32 vcc_lo, vcc_lo, 0
	s_nop 1
	v_writelane_b32 v254, vcc_lo, 63
	s_nop 1
	s_cmp_lt_u32 s61, vcc_lo
	s_cbranch_scc0 .Ldn_entry
	s_mov_b32 vcc_lo, 1
	s_nop 1
	v_writelane_b32 v254, vcc_lo, 62
	s_nop 1
	s_add_u32 s61, s61, vcc_hi
	v_readlane_b32 vcc_lo, v253, 31
	s_nop 1
	s_add_u32 vcc_lo, vcc_lo, vcc_hi
	s_nop 1
	v_writelane_b32 v253, vcc_lo, 31
	s_nop 1
	s_branch .Lgu_restart
.Ldn_entry:
	v_mov_b32_e32 v1, v0
	s_waitcnt lgkmcnt(0)
	s_barrier
	s_nop 0
	v_cmp_gt_i32_e32 vcc, 16, v1
	s_and_saveexec_b64 s[4:5], vcc
	s_cbranch_execz .LBB0_1159
	v_lshlrev_b32_e32 v2, 6, v1
	v_readlane_b32 s6, v254, 22
	v_ashrrev_i32_e32 v3, 31, v2
	v_readlane_b32 s7, v254, 23
	v_cmp_lt_i32_e32 vcc, v235, v240
	s_nop 0
	v_lshl_add_u64 v[2:3], v[2:3], 2, s[6:7]
	global_load_dword v3, v[2:3], off sc1
	v_cndmask_b32_e32 v2, v235, v199, vcc
	v_lshlrev_b32_e32 v2, 2, v2
	v_cmp_lt_i32_e32 vcc, v233, v240
	s_waitcnt vmcnt(0)
	v_add_u32_e32 v4, 0xff, v3
	v_and_b32_e32 v4, 0xffffff00, v4
	ds_bpermute_b32 v2, v2, v4
	v_cndmask_b32_e32 v5, v233, v199, vcc
	v_cmp_lt_i32_e32 vcc, 0, v1
	v_lshlrev_b32_e32 v5, 2, v5
	s_waitcnt lgkmcnt(0)
	v_cndmask_b32_e32 v2, 0, v2, vcc
	v_add_u32_e32 v2, v4, v2
	ds_bpermute_b32 v5, v5, v2
	v_cmp_lt_i32_e32 vcc, v243, v240
	s_nop 1
	v_cndmask_b32_e32 v6, v243, v199, vcc
	v_cmp_lt_i32_e32 vcc, 1, v1
	v_lshlrev_b32_e32 v6, 2, v6
	s_waitcnt lgkmcnt(0)
	v_cndmask_b32_e32 v5, 0, v5, vcc
	v_add_u32_e32 v2, v2, v5
	ds_bpermute_b32 v5, v6, v2
	v_cmp_lt_i32_e32 vcc, v203, v240
	s_nop 1
	v_cndmask_b32_e32 v6, v203, v199, vcc
	v_cmp_lt_i32_e32 vcc, 3, v1
	v_lshlrev_b32_e32 v6, 2, v6
	s_waitcnt lgkmcnt(0)
	v_cndmask_b32_e32 v5, 0, v5, vcc
	v_add_u32_e32 v2, v2, v5
	ds_bpermute_b32 v5, v6, v2
	v_cmp_lt_i32_e32 vcc, 7, v1
	v_lshl_add_u32 v6, v1, 2, 0
	v_add_u32_e32 v6, 0x21e00, v6
	s_waitcnt lgkmcnt(0)
	v_cndmask_b32_e32 v5, 0, v5, vcc
	v_add_u32_e32 v2, v2, v5
	v_sub_u32_e32 v4, v2, v4
	v_cmp_eq_u32_e32 vcc, 15, v1
	ds_write2_b32 v6, v3, v4 offset1:16
	s_and_b64 exec, exec, vcc
	s_cbranch_execz .LBB0_1159
	v_readlane_b32 s2, v253, 58
	s_nop 1
	v_mov_b32_e32 v1, s2
	ds_write_b32 v1, v2

; #define LAS __attribute__((address_space(3)))
;     __device__ __forceinline__ bool next(int i, Unit& u) const {
;         int U = i * G + c, e = 0, found = 0, rem = 0;
;         typedef int i32x4 __attribute__((ext_vector_type(4)));
;         const i32x4 c0 = *(const LAS i32x4*)(seg), c1 = *(const LAS i32x4*)(seg + 4), c2 = *(const LAS i32x4*)(seg + 8), c3 = *(const LAS i32x4*)(seg + 12);
; #pragma unroll
;         for (int k = 0; k < 16; ++k) { const int ck = k < 4 ? c0[k & 3] : k < 8 ? c1[k & 3] : k < 12 ? c2[k & 3] : c3[k & 3];
;             const int nu = ((ck + 255) >> 8) * nct; if (!found) { if (U < nu) { found = 1; e = k; rem = U; } else U -= nu; } }
;         if (!found) return false;
;         e = __builtin_amdgcn_readfirstlane(e); rem = __builtin_amdgcn_readfirstlane(rem);
;         const int rt = rem / nct, ct = rem % nct;
;         u.e = e; u.pm = rt; u.pn = ct; u.rows = seg[e] - rt * 256;
;         u.a = A + (size_t)(seg[16 + e] + rt * 256) * arow_bytes; u.b = Bt + (size_t)e * bexp_bytes + (size_t)ct * btile_bytes; return true;
;     __device__ __forceinline__ void pre(LAS unsigned char* lds, const pg8::Unit& u, int tid) const {
;         const int t = tid & 255, wv = __builtin_amdgcn_readfirstlane(tid >> 6);
;         const void* src = tid < 256 ? (const void*)(list + u.e * NTOK + u.pm * 256 + t) : (const void*)(listw + u.e * NTOK + u.pm * 256 + t);
;         lds_dma4(src, (unsigned)__builtin_amdgcn_readfirstlane((unsigned)(uintptr_t)lds + DNSL_OFF + u.par * 2048 + wv * 256));
;     }
.LBB0_1230:
	s_or_b64 exec, exec, s[24:25]
	s_lshl_b32 s8, s49, 11
	s_and_b32 s8, s8, 0x800
	s_lshl_b32 s9, s26, 2
	s_and_b32 s9, s9, 0xffffff00
	s_add_i32 s54, s8, 0
	s_add_i32 s8, s54, s9
	s_add_i32 s8, s8, 0x22400
	s_mov_b32 s9, m0
	s_mov_b32 m0, s8
	s_nop 0
	global_load_lds_dword v[36:37], off
	s_mov_b32 m0, s9
	v_mov_b32_e32 v34, s42
	ds_read_b128 v[134:137], v34
	s_add_i32 s23, s49, 1
	s_mul_i32 s8, s23, s77
	s_add_i32 s9, s8, s61
	s_cmp_lt_u32 s23, 3
	s_cbranch_scc1 .Ldn_perm_done
	v_readlane_b32 s24, v254, 63
	s_nop 1
	s_cmp_lt_u32 s61, s24
	s_cbranch_scc1 .Ldn_perm_bad
	s_sub_i32 s25, s77, s24
	s_add_i32 s26, s23, -3
	s_mul_i32 s25, s25, s26
	s_sub_i32 s26, s61, s24
	s_add_i32 s25, s25, s26
	s_mul_i32 s26, s77, 3
	s_add_i32 s9, s25, s26
	s_lshl_b32 s26, s77, 2
	s_cmp_lt_u32 s9, s26
	s_cbranch_scc1 .Ldn_perm_done
	v_readlane_b32 s27, v254, 20
	s_nop 1
	s_lshl_b32 s27, s27, 2
	s_add_u32 s27, s27, 0x18000
	s_add_u32 s28, s92, s27
	s_addc_u32 s29, s93, 0
	v_mov_b32_e32 v138, 0
	s_mov_b32 s30, 0
.Ldn_tw_loop:
	global_load_dword v139, v138, s[28:29] sc1
	s_waitcnt vmcnt(0)
	v_readfirstlane_b32 s31, v139
	s_nop 1
	s_cmp_ge_u32 s31, s24
	s_cbranch_scc1 .Ldn_tw_ok
	s_sleep 2
	s_add_u32 s30, s30, 1
	s_cmp_lt_u32 s30, 0x10000
	s_cbranch_scc1 .Ldn_tw_loop
.Ldn_tw_ok:
	buffer_inv sc1
	s_waitcnt vmcnt(0)
	s_branch .Ldn_perm_done
.Ldn_perm_bad:
	s_mov_b32 s9, 0x100000
.Ldn_perm_done:
	v_readlane_b32 s8, v253, 59
	s_waitcnt lgkmcnt(0)
	v_readfirstlane_b32 s68, v136
	v_readfirstlane_b32 s66, v137
	v_mov_b32_e32 v34, s8
	ds_read_b128 v[136:139], v34
	v_readlane_b32 s8, v253, 60
	v_readfirstlane_b32 s26, v135
	s_waitcnt lgkmcnt(0)
	v_readfirstlane_b32 s63, v136
	v_mov_b32_e32 v34, s8
	v_readfirstlane_b32 s62, v137
	v_readfirstlane_b32 s55, v138
	v_readfirstlane_b32 s39, v139
	ds_read_b128 v[136:139], v34
	v_readlane_b32 s8, v253, 61
	s_waitcnt lgkmcnt(0)
	v_readfirstlane_b32 s38, v136
	v_mov_b32_e32 v34, s8
	v_readfirstlane_b32 s8, v134
	s_addk_i32 s8, 0xff
	s_ashr_i32 s8, s8, 6
	v_readfirstlane_b32 s37, v137
	v_readfirstlane_b32 s36, v138
	v_readfirstlane_b32 s35, v139
	ds_read_b128 v[136:139], v34
	s_and_b32 s27, s8, -4
	s_cmp_lt_i32 s9, s27
	s_cselect_b64 s[24:25], -1, 0
	s_and_b64 vcc, s[24:25], exec
	s_cselect_b32 s24, 0, s27
	s_waitcnt lgkmcnt(0)
	v_readfirstlane_b32 s34, v136
	v_readfirstlane_b32 s31, v137
	v_readfirstlane_b32 s30, v138
	v_readfirstlane_b32 s29, v139
	s_mov_b32 s8, 0
	s_sub_i32 s28, s9, s24
	s_mov_b64 s[24:25], 0
	s_cbranch_vccnz .LBB0_1251
	s_addk_i32 s26, 0xff
	s_ashr_i32 s8, s26, 6
	s_and_b32 s8, s8, -4
	s_cmp_lt_i32 s28, s8
	s_cbranch_scc1 .LBB0_1252
	s_sub_i32 s28, s28, s8
	s_mov_b32 s8, 0
	s_mov_b32 s9, 0
	s_branch .LBB0_1253
